# baseline (speedup 1.0000x reference)
_Z14gemm_pc_kernelILi9ELi0EEvPKDF16_S1_PKfS3_S3_PDF16_S4_S4_Pf:
	s_lshl_b32 s4, s2, 1
	s_and_b32 s24, s4, 12
	s_ashr_i32 s4, s2, 6
	s_add_i32 s24, s24, s4
	s_lshl_b32 s4, s2, 3
	v_readfirstlane_b32 s20, v0
	s_and_b32 s4, s4, 8
	s_bfe_u32 s19, s2, 0x30003
	v_and_b32_e32 v142, 63, v0
	s_lshr_b32 s3, s20, 6
	s_or_b32 s21, s4, s19
	s_lshl_b32 s18, s24, 8
	s_mov_b64 s[4:5], -1
	s_cmpk_lt_u32 s20, 0x200
	v_lshrrev_b32_e32 v1, 4, v142
	s_cbranch_scc1 .Lg1_compute

.Lg1_compute:
	v_and_b32_e32 v143, 15, v0
	v_bfe_u32 v2, v0, 1, 3
	s_lshl_b32 s22, s3, 5
	v_xor_b32_e32 v2, v1, v2
	v_or_b32_e32 v3, s22, v143
	v_lshlrev_b32_e32 v3, 7, v3
	v_lshlrev_b32_e32 v2, 4, v2
	s_load_dwordx8 s[4:11], s[0:1], 0x10
	s_load_dwordx4 s[12:15], s[0:1], 0x30
	v_lshlrev_b32_e32 v4, 7, v143
	v_or_b32_e32 v31, v3, v2
	s_waitcnt lgkmcnt(0)
	s_barrier
	v_or_b32_e32 v30, v4, v2
	ds_read_b128 v[82:85], v31 offset:2048
	ds_read_b128 v[14:17], v30 offset:32768
	ds_read_b128 v[26:29], v30 offset:34816
	ds_read_b128 v[46:49], v30 offset:36864
	ds_read_b128 v[58:61], v30 offset:38912
	ds_read_b128 v[70:73], v30 offset:40960
	ds_read_b128 v[86:89], v30 offset:43008
	ds_read_b128 v[90:93], v30 offset:45056
	ds_read_b128 v[94:97], v30 offset:47104
	ds_read_b128 v[98:101], v31
	ds_read_b128 v[102:105], v30 offset:49152
	s_lshr_b32 s23, s2, 3
	v_bitop3_b32 v32, v3, v2, 64 bitop3:0xf6
	v_bitop3_b32 v33, v4, v2, 64 bitop3:0xf6
	ds_read_b128 v[38:41], v32
	ds_read_b128 v[2:5], v32 offset:2048
	ds_read_b128 v[10:13], v33 offset:32768
	s_waitcnt lgkmcnt(4)
	v_mfma_f32_16x16x32_f16 v[6:9], v[14:17], v[98:101], 0
	v_mfma_f32_16x16x32_f16 v[14:17], v[14:17], v[82:85], 0
	ds_read_b128 v[22:25], v33 offset:34816
	v_mfma_f32_16x16x32_f16 v[18:21], v[26:29], v[98:101], 0
	v_mfma_f32_16x16x32_f16 v[26:29], v[26:29], v[82:85], 0
	ds_read_b128 v[42:45], v33 offset:36864
	v_mfma_f32_16x16x32_f16 v[34:37], v[46:49], v[98:101], 0
	v_mfma_f32_16x16x32_f16 v[46:49], v[46:49], v[82:85], 0
	ds_read_b128 v[54:57], v33 offset:38912
	v_mfma_f32_16x16x32_f16 v[50:53], v[58:61], v[98:101], 0
	v_mfma_f32_16x16x32_f16 v[58:61], v[58:61], v[82:85], 0
	ds_read_b128 v[66:69], v33 offset:40960
	v_mfma_f32_16x16x32_f16 v[62:65], v[70:73], v[98:101], 0
	v_mfma_f32_16x16x32_f16 v[70:73], v[70:73], v[82:85], 0
	ds_read_b128 v[78:81], v33 offset:43008
	v_mfma_f32_16x16x32_f16 v[74:77], v[86:89], v[98:101], 0
	v_mfma_f32_16x16x32_f16 v[86:89], v[86:89], v[82:85], 0
	ds_read_b128 v[110:113], v33 offset:45056
	v_mfma_f32_16x16x32_f16 v[106:109], v[90:93], v[98:101], 0
	v_mfma_f32_16x16x32_f16 v[114:117], v[90:93], v[82:85], 0
	ds_read_b128 v[122:125], v33 offset:47104
	v_mfma_f32_16x16x32_f16 v[118:121], v[94:97], v[98:101], 0
	v_mfma_f32_16x16x32_f16 v[126:129], v[94:97], v[82:85], 0
	ds_read_b128 v[134:137], v33 offset:49152
	s_waitcnt lgkmcnt(11)
	v_mfma_f32_16x16x32_f16 v[130:133], v[102:105], v[98:101], 0
	v_mfma_f32_16x16x32_f16 v[138:141], v[102:105], v[82:85], 0
	s_mov_b32 s17, 0xc800
	s_mov_b32 s16, 27

.LBB2_36:
	s_lshr_b32 s4, s21, 2
	s_or_b32 s4, s8, s4
	s_lshr_b32 s6, s18, 5
	s_ashr_i32 s5, s4, 31
	s_or_b32 s6, s3, s6
	s_lshl_b64 s[4:5], s[4:5], 6
	s_and_b32 s6, s6, 62
	s_waitcnt lgkmcnt(0)
	global_store_dwordx4 v[6:7], v[2:5], off sc0 sc1
	v_lshrrev_b32_e32 v6, 1, v142
	s_or_b32 s4, s4, s6
	v_and_b32_e32 v2, 1, v0
	s_bfe_u32 s6, s23, 0x10001
	v_mul_u32_u24_e32 v3, 0x130, v6
	v_lshlrev_b32_e32 v10, 4, v2
	s_or_b32 s4, s4, s6
	v_add3_u32 v2, s25, v3, v10
	s_lshl_b64 s[4:5], s[4:5], 12
	ds_read_b128 v[2:5], v2 offset:256
	v_and_or_b32 v6, s22, 32, v6
	s_add_u32 s4, s14, s4
	s_addc_u32 s5, s15, s5
	v_lshlrev_b32_e32 v6, 6, v6
	v_mov_b32_e32 v7, 0
	v_lshl_add_u64 v[8:9], s[4:5], 0, v[6:7]
	s_lshl_b32 s4, s23, 5
	v_and_or_b32 v6, s4, 32, v10
	v_lshl_add_u64 v[6:7], v[8:9], 0, v[6:7]
	s_waitcnt lgkmcnt(0)
	global_store_dwordx4 v[6:7], v[2:5], off sc0 sc1
	s_mov_b64 s[4:5], 0
	s_endpgm
	.p2align	8

_Z14gemm_pc_kernelILi7ELi1EEvPKDF16_S1_PKfS3_S3_PDF16_S4_S4_Pf:
	s_lshl_b32 s4, s2, 1
	s_and_b32 s4, s4, 12
	s_lshr_b32 s5, s2, 6
	s_add_i32 s4, s4, s5
	s_lshl_b32 s5, s2, 3
	v_readfirstlane_b32 s8, v0
	s_and_b32 s5, s5, 8
	s_bfe_u32 s10, s2, 0x30003
	v_and_b32_e32 v1, 63, v0
	s_lshr_b32 s3, s8, 6
	s_or_b32 s11, s5, s10
	s_lshl_b32 s9, s4, 8
	s_mov_b64 s[4:5], -1
	s_cmpk_lt_u32 s8, 0x200
	v_lshrrev_b32_e32 v102, 4, v1
	s_cbranch_scc1 .Lg2_compute

.Lg2_compute:
	v_and_b32_e32 v103, 15, v0
	v_bfe_u32 v2, v0, 1, 3
	s_lshl_b32 s12, s3, 5
	v_xor_b32_e32 v2, v102, v2
	v_or_b32_e32 v3, s12, v103
	v_lshlrev_b32_e32 v3, 7, v3
	v_lshlrev_b32_e32 v2, 4, v2
	s_load_dwordx2 s[4:5], s[0:1], 0x40
	s_load_dwordx2 s[6:7], s[0:1], 0x10
	v_lshlrev_b32_e32 v4, 7, v103
	v_or_b32_e32 v31, v3, v2
	s_waitcnt lgkmcnt(0)
	s_barrier
	v_or_b32_e32 v30, v4, v2
	ds_read_b128 v[34:37], v31 offset:2048
	ds_read_b128 v[10:13], v30 offset:32768
	ds_read_b128 v[22:25], v30 offset:34816
	ds_read_b128 v[46:49], v30 offset:36864
	ds_read_b128 v[62:65], v30 offset:38912
	ds_read_b128 v[74:77], v30 offset:40960
	ds_read_b128 v[86:89], v30 offset:43008
	ds_read_b128 v[90:93], v31
	ds_read_b128 v[98:101], v30 offset:45056
	v_bitop3_b32 v32, v3, v2, 64 bitop3:0xf6
	v_bitop3_b32 v33, v4, v2, 64 bitop3:0xf6
	ds_read_b128 v[54:57], v32
	ds_read_b128 v[26:29], v32 offset:2048
	ds_read_b128 v[6:9], v33 offset:32768
	s_waitcnt lgkmcnt(4)
	v_mfma_f32_16x16x32_f16 v[2:5], v[10:13], v[90:93], 0
	v_mfma_f32_16x16x32_f16 v[10:13], v[10:13], v[34:37], 0
	ds_read_b128 v[18:21], v33 offset:34816
	v_mfma_f32_16x16x32_f16 v[14:17], v[22:25], v[90:93], 0
	v_mfma_f32_16x16x32_f16 v[22:25], v[22:25], v[34:37], 0
	ds_read_b128 v[42:45], v33 offset:36864
	v_mfma_f32_16x16x32_f16 v[38:41], v[46:49], v[90:93], 0
	v_mfma_f32_16x16x32_f16 v[46:49], v[46:49], v[34:37], 0
	ds_read_b128 v[58:61], v33 offset:38912
	v_mfma_f32_16x16x32_f16 v[50:53], v[62:65], v[90:93], 0
	v_mfma_f32_16x16x32_f16 v[62:65], v[62:65], v[34:37], 0
	ds_read_b128 v[70:73], v33 offset:40960
	v_mfma_f32_16x16x32_f16 v[66:69], v[74:77], v[90:93], 0
	v_mfma_f32_16x16x32_f16 v[74:77], v[74:77], v[34:37], 0
	ds_read_b128 v[82:85], v33 offset:43008
	v_mfma_f32_16x16x32_f16 v[78:81], v[86:89], v[90:93], 0
	v_mfma_f32_16x16x32_f16 v[86:89], v[86:89], v[34:37], 0
	ds_read_b128 v[94:97], v33 offset:45056
	s_waitcnt lgkmcnt(9)
	v_mfma_f32_16x16x32_f16 v[90:93], v[98:101], v[90:93], 0
	v_mfma_f32_16x16x32_f16 v[98:101], v[98:101], v[34:37], 0
	s_mov_b32 s14, 0xb800
	s_mov_b32 s13, 27
.LBB3_2:
	s_waitcnt lgkmcnt(0)
	s_barrier
	v_add_u32_e32 v104, s14, v31
	ds_read_b128 v[34:37], v104
	ds_read_b128 v[104:107], v104 offset:2048
	v_add_u32_e32 v132, s14, v30
	v_mfma_f32_16x16x32_f16 v[2:5], v[6:9], v[54:57], v[2:5]
	ds_read_b128 v[108:111], v132 offset:32768
	v_mfma_f32_16x16x32_f16 v[10:13], v[6:9], v[26:29], v[10:13]
	v_mfma_f32_16x16x32_f16 v[14:17], v[18:21], v[54:57], v[14:17]
	ds_read_b128 v[112:115], v132 offset:34816
	v_mfma_f32_16x16x32_f16 v[22:25], v[18:21], v[26:29], v[22:25]
	v_mfma_f32_16x16x32_f16 v[38:41], v[42:45], v[54:57], v[38:41]
	ds_read_b128 v[116:119], v132 offset:36864
	v_mfma_f32_16x16x32_f16 v[46:49], v[42:45], v[26:29], v[46:49]
	v_mfma_f32_16x16x32_f16 v[50:53], v[58:61], v[54:57], v[50:53]
	ds_read_b128 v[120:123], v132 offset:38912
	v_mfma_f32_16x16x32_f16 v[62:65], v[58:61], v[26:29], v[62:65]
	v_mfma_f32_16x16x32_f16 v[66:69], v[70:73], v[54:57], v[66:69]
	ds_read_b128 v[124:127], v132 offset:40960
	v_mfma_f32_16x16x32_f16 v[74:77], v[70:73], v[26:29], v[74:77]
	v_mfma_f32_16x16x32_f16 v[78:81], v[82:85], v[54:57], v[78:81]
	ds_read_b128 v[128:131], v132 offset:43008
	v_mfma_f32_16x16x32_f16 v[86:89], v[82:85], v[26:29], v[86:89]
	v_mfma_f32_16x16x32_f16 v[90:93], v[94:97], v[54:57], v[90:93]
	ds_read_b128 v[132:135], v132 offset:45056
	v_mfma_f32_16x16x32_f16 v[98:101], v[94:97], v[26:29], v[98:101]
	v_add_u32_e32 v6, s14, v32
	v_add_u32_e32 v94, s14, v33
	ds_read_b128 v[54:57], v6
	ds_read_b128 v[26:29], v6 offset:2048
	ds_read_b128 v[6:9], v94 offset:32768
	s_waitcnt lgkmcnt(9)
	v_mfma_f32_16x16x32_f16 v[2:5], v[108:111], v[34:37], v[2:5]
	v_mfma_f32_16x16x32_f16 v[10:13], v[108:111], v[104:107], v[10:13]
	ds_read_b128 v[18:21], v94 offset:34816
	s_waitcnt lgkmcnt(9)
	v_mfma_f32_16x16x32_f16 v[14:17], v[112:115], v[34:37], v[14:17]
	v_mfma_f32_16x16x32_f16 v[22:25], v[112:115], v[104:107], v[22:25]
	ds_read_b128 v[42:45], v94 offset:36864
	s_waitcnt lgkmcnt(9)
	v_mfma_f32_16x16x32_f16 v[38:41], v[116:119], v[34:37], v[38:41]
	v_mfma_f32_16x16x32_f16 v[46:49], v[116:119], v[104:107], v[46:49]
	ds_read_b128 v[58:61], v94 offset:38912
	s_waitcnt lgkmcnt(9)
	v_mfma_f32_16x16x32_f16 v[50:53], v[120:123], v[34:37], v[50:53]
	v_mfma_f32_16x16x32_f16 v[62:65], v[120:123], v[104:107], v[62:65]
	ds_read_b128 v[70:73], v94 offset:40960
	s_waitcnt lgkmcnt(9)
	v_mfma_f32_16x16x32_f16 v[66:69], v[124:127], v[34:37], v[66:69]
	v_mfma_f32_16x16x32_f16 v[74:77], v[124:127], v[104:107], v[74:77]
	ds_read_b128 v[82:85], v94 offset:43008
	s_waitcnt lgkmcnt(9)
	v_mfma_f32_16x16x32_f16 v[78:81], v[128:131], v[34:37], v[78:81]
	v_mfma_f32_16x16x32_f16 v[86:89], v[128:131], v[104:107], v[86:89]
	ds_read_b128 v[94:97], v94 offset:45056
	s_waitcnt lgkmcnt(9)
	v_mfma_f32_16x16x32_f16 v[90:93], v[132:135], v[34:37], v[90:93]
	v_mfma_f32_16x16x32_f16 v[98:101], v[132:135], v[104:107], v[98:101]
	s_add_i32 s15, s14, 0xb800
	s_cmp_lg_u32 s14, 0x17000
	s_cselect_b32 s14, s15, 0
	s_add_i32 s13, s13, -1
	s_cmp_eq_u32 s13, 0
	s_cbranch_scc0 .LBB3_2
	s_waitcnt lgkmcnt(6)
	v_mfma_f32_16x16x32_f16 v[30:33], v[6:9], v[54:57], v[2:5]
	v_mfma_f32_16x16x32_f16 v[2:5], v[6:9], v[26:29], v[10:13]
	s_waitcnt lgkmcnt(5)
	v_mfma_f32_16x16x32_f16 v[34:37], v[18:21], v[54:57], v[14:17]
	v_mfma_f32_16x16x32_f16 v[6:9], v[18:21], v[26:29], v[22:25]
	s_waitcnt lgkmcnt(4)
	v_mfma_f32_16x16x32_f16 v[38:41], v[42:45], v[54:57], v[38:41]
	v_mfma_f32_16x16x32_f16 v[10:13], v[42:45], v[26:29], v[46:49]
	s_waitcnt lgkmcnt(3)
	v_mfma_f32_16x16x32_f16 v[42:45], v[58:61], v[54:57], v[50:53]
	v_mfma_f32_16x16x32_f16 v[14:17], v[58:61], v[26:29], v[62:65]
	s_waitcnt lgkmcnt(2)
	v_mfma_f32_16x16x32_f16 v[46:49], v[70:73], v[54:57], v[66:69]
	v_mfma_f32_16x16x32_f16 v[18:21], v[70:73], v[26:29], v[74:77]
	s_waitcnt lgkmcnt(1)
	v_mfma_f32_16x16x32_f16 v[50:53], v[82:85], v[54:57], v[78:81]
	v_mfma_f32_16x16x32_f16 v[22:25], v[82:85], v[26:29], v[86:89]
	s_waitcnt lgkmcnt(0)
	v_mfma_f32_16x16x32_f16 v[54:57], v[94:97], v[54:57], v[90:93]
	v_mfma_f32_16x16x32_f16 v[26:29], v[94:97], v[26:29], v[98:101]
	s_mul_i32 s14, s11, 0x1c0
	s_add_u32 s6, s6, s14
	s_waitcnt lgkmcnt(0)
	s_barrier
	s_addc_u32 s7, s7, 0
	v_lshlrev_b32_e32 v78, 4, v102
	global_load_dwordx4 v[58:61], v78, s[6:7]
	global_load_dwordx4 v[62:65], v78, s[6:7] offset:64
	global_load_dwordx4 v[66:69], v78, s[6:7] offset:128
	global_load_dwordx4 v[70:73], v78, s[6:7] offset:192
	global_load_dwordx4 v[74:77], v78, s[6:7] offset:256
	global_load_dwordx4 v[82:85], v78, s[6:7] offset:320
	global_load_dwordx4 v[86:89], v78, s[6:7] offset:384
	s_mul_i32 s6, s3, 0x3a00
	v_mul_u32_u24_e32 v78, 0x1d0, v103
	v_and_b32_e32 v80, 48, v0
	v_mul_lo_u16_e32 v81, 37, v1
	v_or_b32_e32 v90, 64, v1
	v_add3_u32 v93, s6, v78, v80
	v_lshrrev_b16_e32 v78, 10, v81
	s_or_b32 s12, s12, s9
	v_mul_lo_u16_e32 v80, 0x93, v90
	v_mul_lo_u16_e32 v81, 28, v78
	s_add_u32 s4, s4, s14
	v_mov_b32_e32 v92, 4
	v_lshrrev_b16_e32 v80, 12, v80
	v_sub_u16_e32 v81, v1, v81
	s_addc_u32 s5, s5, 0
	s_movk_i32 s13, 0x1c00
	v_mul_u32_u24_e32 v91, 0x1d0, v78
	v_or_b32_e32 v94, s12, v78
	v_mul_lo_u16_e32 v95, 28, v80
	v_mul_u32_u24_e32 v96, 0x1d0, v80
	v_or_b32_e32 v97, s12, v80
	v_lshlrev_b32_sdwa v78, v92, v81 dst_sel:DWORD dst_unused:UNUSED_PAD src0_sel:DWORD src1_sel:BYTE_0
	v_mov_b64_e32 v[80:81], s[4:5]
	v_mov_b32_e32 v79, 0
	v_sub_u16_e32 v95, v90, v95
	v_add3_u32 v98, s6, v91, v78
	v_mad_i64_i32 v[90:91], s[4:5], v94, s13, v[80:81]
	v_lshl_add_u64 v[90:91], v[90:91], 0, v[78:79]
	v_lshlrev_b32_sdwa v78, v92, v95 dst_sel:DWORD dst_unused:UNUSED_PAD src0_sel:DWORD src1_sel:BYTE_0
	s_movk_i32 s7, 0x1d0
	s_mov_b32 s14, 0x7060302
	s_waitcnt vmcnt(6)
	v_pk_add_f32 v[32:33], v[32:33], v[60:61]
	v_pk_add_f32 v[30:31], v[30:31], v[58:59]
	s_waitcnt vmcnt(5)
	v_pk_add_f32 v[36:37], v[36:37], v[64:65]
	v_pk_add_f32 v[34:35], v[34:35], v[62:63]
	s_waitcnt vmcnt(4)
	v_pk_add_f32 v[40:41], v[40:41], v[68:69]
	v_pk_add_f32 v[38:39], v[38:39], v[66:67]
	s_waitcnt vmcnt(3)
	v_pk_add_f32 v[44:45], v[44:45], v[72:73]
	v_pk_add_f32 v[42:43], v[42:43], v[70:71]
	s_waitcnt vmcnt(2)
	v_pk_add_f32 v[48:49], v[48:49], v[76:77]
	v_pk_add_f32 v[46:47], v[46:47], v[74:75]
	s_waitcnt vmcnt(1)
	v_pk_add_f32 v[52:53], v[52:53], v[84:85]
	v_pk_add_f32 v[50:51], v[50:51], v[82:83]
	s_waitcnt vmcnt(0)
	v_pk_add_f32 v[56:57], v[56:57], v[88:89]
	v_pk_add_f32 v[54:55], v[54:55], v[86:87]
	v_pk_add_f32 v[4:5], v[4:5], v[60:61]
	v_pk_add_f32 v[2:3], v[2:3], v[58:59]
	v_pk_add_f32 v[8:9], v[8:9], v[64:65]
	v_pk_add_f32 v[6:7], v[6:7], v[62:63]
	v_pk_add_f32 v[12:13], v[12:13], v[68:69]
	v_pk_add_f32 v[10:11], v[10:11], v[66:67]
	v_pk_add_f32 v[16:17], v[16:17], v[72:73]
	v_pk_add_f32 v[14:15], v[14:15], v[70:71]
	v_pk_add_f32 v[20:21], v[20:21], v[76:77]
	v_pk_add_f32 v[18:19], v[18:19], v[74:75]
	v_pk_add_f32 v[24:25], v[24:25], v[84:85]
	v_pk_add_f32 v[22:23], v[22:23], v[82:83]
	v_pk_add_f32 v[28:29], v[28:29], v[88:89]
	v_pk_add_f32 v[26:27], v[26:27], v[86:87]
	ds_write_b128 v93, v[30:33]
	ds_write_b128 v93, v[34:37] offset:64
	ds_write_b128 v93, v[38:41] offset:128
	ds_write_b128 v93, v[42:45] offset:192
	ds_write_b128 v93, v[46:49] offset:256
	ds_write_b128 v93, v[50:53] offset:320
	ds_write_b128 v93, v[54:57] offset:384
	ds_write_b128 v93, v[2:5] offset:7424
	ds_write_b128 v93, v[6:9] offset:7488
	ds_write_b128 v93, v[10:13] offset:7552
	ds_write_b128 v93, v[14:17] offset:7616
	ds_write_b128 v93, v[18:21] offset:7680
	ds_write_b128 v93, v[22:25] offset:7744
	ds_write_b128 v93, v[26:29] offset:7808
	s_waitcnt lgkmcnt(0)
	ds_read_b128 v[2:5], v98
	v_add3_u32 v6, s6, v96, v78
	ds_read_b128 v[6:9], v6
	v_mad_i64_i32 v[10:11], s[4:5], v97, s13, v[80:81]
	s_waitcnt lgkmcnt(1)
	global_store_dwordx4 v[90:91], v[2:5], off sc0 sc1
	s_movk_i32 s4, 0xbc
	v_mov_b32_e32 v12, 28
	v_lshl_add_u64 v[2:3], v[10:11], 0, v[78:79]
	s_waitcnt lgkmcnt(0)
	global_store_dwordx4 v[2:3], v[6:9], off sc0 sc1
	v_mov_b32_e32 v2, 0xffffff80
	v_bitop3_b16 v2, v1, s4, v2 bitop3:0xc8
	v_lshrrev_b16_e32 v2, 2, v2
	v_mul_lo_u16_e32 v6, 37, v2
	v_or_b32_e32 v3, 0xffffff80, v1
	v_mul_lo_u16_sdwa v2, v6, v12 dst_sel:DWORD dst_unused:UNUSED_PAD src0_sel:BYTE_1 src1_sel:DWORD
	v_sub_u16_e32 v2, v3, v2
	v_mul_u32_u24_sdwa v3, v6, s7 dst_sel:DWORD dst_unused:UNUSED_PAD src0_sel:BYTE_1 src1_sel:DWORD
	v_or_b32_sdwa v6, s12, v6 dst_sel:DWORD dst_unused:UNUSED_PAD src0_sel:DWORD src1_sel:BYTE_1
	v_lshlrev_b32_sdwa v78, v92, v2 dst_sel:DWORD dst_unused:UNUSED_PAD src0_sel:DWORD src1_sel:BYTE_0
	v_mad_i64_i32 v[6:7], s[4:5], v6, s13, v[80:81]
	v_lshl_add_u64 v[10:11], v[6:7], 0, v[78:79]
	v_or_b32_e32 v6, 0xffffffc0, v1
	v_lshrrev_b16_e32 v7, 2, v6
	v_and_b32_e32 v7, 63, v7
	v_mul_lo_u16_e32 v13, 37, v7
	v_add3_u32 v2, s6, v3, v78
	v_mul_lo_u16_sdwa v7, v13, v12 dst_sel:DWORD dst_unused:UNUSED_PAD src0_sel:BYTE_1 src1_sel:DWORD
	ds_read_b128 v[2:5], v2
	v_sub_u16_e32 v6, v6, v7
	v_mul_u32_u24_sdwa v7, v13, s7 dst_sel:DWORD dst_unused:UNUSED_PAD src0_sel:BYTE_1 src1_sel:DWORD
	v_lshlrev_b32_sdwa v78, v92, v6 dst_sel:DWORD dst_unused:UNUSED_PAD src0_sel:DWORD src1_sel:BYTE_0
	v_add3_u32 v6, s6, v7, v78
	ds_read_b128 v[6:9], v6
	s_waitcnt lgkmcnt(1)
	global_store_dwordx4 v[10:11], v[2:5], off sc0 sc1
	s_nop 1
	v_or_b32_sdwa v2, s12, v13 dst_sel:DWORD dst_unused:UNUSED_PAD src0_sel:DWORD src1_sel:BYTE_1
	v_mad_i64_i32 v[2:3], s[4:5], v2, s13, v[80:81]
	v_lshl_add_u64 v[2:3], v[2:3], 0, v[78:79]
	s_waitcnt lgkmcnt(0)
	global_store_dwordx4 v[2:3], v[6:9], off sc0 sc1
	v_or_b32_e32 v3, 0x100, v1
	v_or_b32_e32 v2, 0x140, v1
	v_mul_u32_u24_e32 v6, 0x925, v3
	v_mul_lo_u16_sdwa v4, v6, v12 dst_sel:DWORD dst_unused:UNUSED_PAD src0_sel:WORD_1 src1_sel:DWORD
	v_sub_u16_e32 v3, v3, v4
	v_mul_u32_u24_e32 v13, 0x925, v2
	v_lshlrev_b32_e32 v78, 4, v3
	v_mul_lo_u16_sdwa v3, v13, v12 dst_sel:DWORD dst_unused:UNUSED_PAD src0_sel:WORD_1 src1_sel:DWORD
	v_sub_u16_e32 v8, v2, v3
	v_perm_b32 v2, v13, v6, s14
	v_pk_mul_lo_u16 v9, v2, s7 op_sel_hi:[1,0]
	v_or_b32_sdwa v6, s12, v6 dst_sel:DWORD dst_unused:UNUSED_PAD src0_sel:DWORD src1_sel:WORD_1
	v_and_b32_e32 v2, 0xfff0, v9
	v_add3_u32 v2, s6, v2, v78
	ds_read_b128 v[2:5], v2
	v_mad_i64_i32 v[6:7], s[4:5], v6, s13, v[80:81]
	v_lshl_add_u64 v[10:11], v[6:7], 0, v[78:79]
	v_lshrrev_b32_e32 v6, 16, v9
	v_lshlrev_b32_e32 v78, 4, v8
	v_add3_u32 v6, s6, v6, v78
	ds_read_b128 v[6:9], v6
	s_waitcnt lgkmcnt(1)
	global_store_dwordx4 v[10:11], v[2:5], off sc0 sc1
	s_nop 1
	v_or_b32_sdwa v2, s12, v13 dst_sel:DWORD dst_unused:UNUSED_PAD src0_sel:DWORD src1_sel:WORD_1
	v_mad_i64_i32 v[2:3], s[4:5], v2, s13, v[80:81]
	v_lshl_add_u64 v[2:3], v[2:3], 0, v[78:79]
	s_waitcnt lgkmcnt(0)
	global_store_dwordx4 v[2:3], v[6:9], off sc0 sc1
	v_or_b32_e32 v3, 0x180, v1
	v_or_b32_e32 v2, 0x1c0, v1
	v_mul_u32_u24_e32 v6, 0x925, v3
	v_mul_lo_u16_sdwa v4, v6, v12 dst_sel:DWORD dst_unused:UNUSED_PAD src0_sel:WORD_1 src1_sel:DWORD
	v_sub_u16_e32 v3, v3, v4
	v_mul_u32_u24_e32 v13, 0x925, v2
	v_lshlrev_b32_e32 v78, 4, v3
	v_mul_lo_u16_sdwa v3, v13, v12 dst_sel:DWORD dst_unused:UNUSED_PAD src0_sel:WORD_1 src1_sel:DWORD
	v_sub_u16_e32 v8, v2, v3
	v_perm_b32 v2, v13, v6, s14
	v_pk_mul_lo_u16 v9, v2, s7 op_sel_hi:[1,0]
	v_or_b32_sdwa v6, s12, v6 dst_sel:DWORD dst_unused:UNUSED_PAD src0_sel:DWORD src1_sel:WORD_1
	v_and_b32_e32 v2, 0xfff0, v9
	v_add3_u32 v2, s6, v2, v78
	ds_read_b128 v[2:5], v2
	v_mad_i64_i32 v[6:7], s[4:5], v6, s13, v[80:81]
	v_lshl_add_u64 v[10:11], v[6:7], 0, v[78:79]
	v_lshrrev_b32_e32 v6, 16, v9
	v_lshlrev_b32_e32 v78, 4, v8
	v_add3_u32 v6, s6, v6, v78
	ds_read_b128 v[6:9], v6
	s_waitcnt lgkmcnt(1)
	global_store_dwordx4 v[10:11], v[2:5], off sc0 sc1
	s_nop 1
	v_or_b32_sdwa v2, s12, v13 dst_sel:DWORD dst_unused:UNUSED_PAD src0_sel:DWORD src1_sel:WORD_1
	v_mad_i64_i32 v[2:3], s[4:5], v2, s13, v[80:81]
	v_lshl_add_u64 v[2:3], v[2:3], 0, v[78:79]
	s_waitcnt lgkmcnt(0)
	global_store_dwordx4 v[2:3], v[6:9], off sc0 sc1
	v_or_b32_e32 v3, 0x200, v1
	v_or_b32_e32 v2, 0x240, v1
	v_mul_u32_u24_e32 v6, 0x925, v3
	v_mul_lo_u16_sdwa v4, v6, v12 dst_sel:DWORD dst_unused:UNUSED_PAD src0_sel:WORD_1 src1_sel:DWORD
	v_sub_u16_e32 v3, v3, v4
	v_mul_u32_u24_e32 v13, 0x925, v2
	v_lshlrev_b32_e32 v78, 4, v3
	v_mul_lo_u16_sdwa v3, v13, v12 dst_sel:DWORD dst_unused:UNUSED_PAD src0_sel:WORD_1 src1_sel:DWORD
	v_sub_u16_e32 v8, v2, v3
	v_perm_b32 v2, v13, v6, s14
	v_pk_mul_lo_u16 v9, v2, s7 op_sel_hi:[1,0]
	v_or_b32_sdwa v6, s12, v6 dst_sel:DWORD dst_unused:UNUSED_PAD src0_sel:DWORD src1_sel:WORD_1
	v_and_b32_e32 v2, 0xfff0, v9
	v_add3_u32 v2, s6, v2, v78
	ds_read_b128 v[2:5], v2
	v_mad_i64_i32 v[6:7], s[4:5], v6, s13, v[80:81]
	v_lshl_add_u64 v[10:11], v[6:7], 0, v[78:79]
	v_lshrrev_b32_e32 v6, 16, v9
	v_lshlrev_b32_e32 v78, 4, v8
	v_add3_u32 v6, s6, v6, v78
	ds_read_b128 v[6:9], v6
	s_waitcnt lgkmcnt(1)
	global_store_dwordx4 v[10:11], v[2:5], off sc0 sc1
	s_nop 1
	v_or_b32_sdwa v2, s12, v13 dst_sel:DWORD dst_unused:UNUSED_PAD src0_sel:DWORD src1_sel:WORD_1
	v_mad_i64_i32 v[2:3], s[4:5], v2, s13, v[80:81]
	v_lshl_add_u64 v[2:3], v[2:3], 0, v[78:79]
	s_waitcnt lgkmcnt(0)
	global_store_dwordx4 v[2:3], v[6:9], off sc0 sc1
	v_or_b32_e32 v3, 0x280, v1
	v_or_b32_e32 v2, 0x2c0, v1
	v_mul_u32_u24_e32 v6, 0x925, v3
	v_mul_lo_u16_sdwa v4, v6, v12 dst_sel:DWORD dst_unused:UNUSED_PAD src0_sel:WORD_1 src1_sel:DWORD
	v_sub_u16_e32 v3, v3, v4
	v_mul_u32_u24_e32 v13, 0x925, v2
	v_lshlrev_b32_e32 v78, 4, v3
	v_mul_lo_u16_sdwa v3, v13, v12 dst_sel:DWORD dst_unused:UNUSED_PAD src0_sel:WORD_1 src1_sel:DWORD
	v_sub_u16_e32 v8, v2, v3
	v_perm_b32 v2, v13, v6, s14
	v_pk_mul_lo_u16 v9, v2, s7 op_sel_hi:[1,0]
	v_or_b32_sdwa v6, s12, v6 dst_sel:DWORD dst_unused:UNUSED_PAD src0_sel:DWORD src1_sel:WORD_1
	v_and_b32_e32 v2, 0xfff0, v9
	v_add3_u32 v2, s6, v2, v78
	ds_read_b128 v[2:5], v2
	v_mad_i64_i32 v[6:7], s[4:5], v6, s13, v[80:81]
	v_lshl_add_u64 v[10:11], v[6:7], 0, v[78:79]
	v_lshrrev_b32_e32 v6, 16, v9
	v_lshlrev_b32_e32 v78, 4, v8
	v_add3_u32 v6, s6, v6, v78
	ds_read_b128 v[6:9], v6
	s_waitcnt lgkmcnt(1)
	global_store_dwordx4 v[10:11], v[2:5], off sc0 sc1
	s_nop 1
	v_or_b32_sdwa v2, s12, v13 dst_sel:DWORD dst_unused:UNUSED_PAD src0_sel:DWORD src1_sel:WORD_1
	v_mad_i64_i32 v[2:3], s[4:5], v2, s13, v[80:81]
	v_lshl_add_u64 v[2:3], v[2:3], 0, v[78:79]
	s_waitcnt lgkmcnt(0)
	global_store_dwordx4 v[2:3], v[6:9], off sc0 sc1
	v_or_b32_e32 v3, 0x300, v1
	v_or_b32_e32 v2, 0x340, v1
	v_mul_u32_u24_e32 v6, 0x925, v3
	v_mul_lo_u16_sdwa v4, v6, v12 dst_sel:DWORD dst_unused:UNUSED_PAD src0_sel:WORD_1 src1_sel:DWORD
	v_sub_u16_e32 v3, v3, v4
	v_mul_u32_u24_e32 v13, 0x925, v2
	v_lshlrev_b32_e32 v78, 4, v3
	v_mul_lo_u16_sdwa v3, v13, v12 dst_sel:DWORD dst_unused:UNUSED_PAD src0_sel:WORD_1 src1_sel:DWORD
	v_sub_u16_e32 v8, v2, v3
	v_perm_b32 v2, v13, v6, s14
	v_pk_mul_lo_u16 v9, v2, s7 op_sel_hi:[1,0]
	v_or_b32_sdwa v6, s12, v6 dst_sel:DWORD dst_unused:UNUSED_PAD src0_sel:DWORD src1_sel:WORD_1
	v_and_b32_e32 v2, 0xfff0, v9
	v_add3_u32 v2, s6, v2, v78
	ds_read_b128 v[2:5], v2
	v_mad_i64_i32 v[6:7], s[4:5], v6, s13, v[80:81]
	v_lshl_add_u64 v[10:11], v[6:7], 0, v[78:79]
	v_lshrrev_b32_e32 v6, 16, v9
	v_lshlrev_b32_e32 v78, 4, v8
	v_add3_u32 v6, s6, v6, v78
	ds_read_b128 v[6:9], v6
	s_waitcnt lgkmcnt(1)
	global_store_dwordx4 v[10:11], v[2:5], off sc0 sc1
	s_nop 1
	v_or_b32_sdwa v2, s12, v13 dst_sel:DWORD dst_unused:UNUSED_PAD src0_sel:DWORD src1_sel:WORD_1
	v_mad_i64_i32 v[2:3], s[4:5], v2, s13, v[80:81]
	v_lshl_add_u64 v[2:3], v[2:3], 0, v[78:79]
	s_mov_b64 s[4:5], 0
	s_waitcnt lgkmcnt(0)
	global_store_dwordx4 v[2:3], v[6:9], off sc0 sc1
	s_endpgm
	.p2align	8
